# v29 plus XCD-contiguous unit deal for the phase-12 attention units (window: one (batch, kv head) per XCD; NA: 4 heads x 8 row groups of one batch)
# speedup vs baseline: 1.0263x; 1.0008x over previous
; #define LAS __attribute__((address_space(3)))
; #define SEAM(k) do { if (rep_ == REP(k) && IN((k) + 1)) xcd_barrier(bar); } while (0)
; DI void phase_attn_win(const Params& p, LAS unsigned char* lds, int G, int bid) {
;     const int tid = threadIdx.x, lane = tid & 63, wave = __builtin_amdgcn_readfirstlane(tid >> 6), h = lane >> 5;
;     const bf16_t* Z = (const bf16_t*)(p.ws + WS_Z);
;     bf16_t* Y = (bf16_t*)(p.ws + WS_Y);
;     const float c2 = 0.08838834764831845f * LOG2E;
;     const AtRd rd = at_rd_init<128>(lane);
;     const AtDma dm = at_dma_init<128>(L1IN * 2, wave, lane);
;     for (int u = bid; u < 256; u += G) {
;         WinDrv T; T.Z = (const char*)Z; T.b = u >> 6; T.kvh = (u >> 5) & 1; const int blk = u & 31; T.k0base = 64 * blk - 128;
;         const int head = T.kvh * 4 + (wave >> 1), qpos = 64 * blk + 32 * (wave & 1) + (lane & 31), qrow = NCTX + T.b * SEQ + qpos;
;         T.qpos = qpos;
;         bf16x8 qf[8];
; #pragma unroll
;         for (int s = 0; s < 8; ++s) qf[s] = *(const bf16x8*)(Z + (size_t)qrow * L1IN + head * 128 + 16 * s + 8 * h);
; __global__ void __launch_bounds__(NTHREADS, 2) fwd_kernel(Params p) {
;     ...
;     if (IN(12)) for (int rep_ = 0; rep_ <= REP(12); ++rep_) { if (rep_) __syncthreads(); if (!(p.flags & 2)) phase_attn_win(p, lds, G, bid); __syncthreads(); if (!(p.flags & 4)) phase_attn_na(p, lds, G, bid); SEAM(12); }
.LBB0_1337:
	s_cmp_gt_i32 s24, 12
	s_cselect_b64 s[0:1], -1, 0
	s_cmp_lt_i32 s25, 13
	s_cselect_b64 s[2:3], -1, 0
	s_or_b64 s[0:1], s[0:1], s[2:3]
	s_and_b64 vcc, exec, s[0:1]
	s_cbranch_vccnz .LBB0_1431
	s_and_b32 s98, s22, 7
	s_lshl_b32 s98, s98, 5
	s_lshr_b32 s99, s22, 3
	s_or_b32 s98, s98, s99
	s_cmpk_lg_i32 s23, 0x100
	s_cselect_b32 s98, s22, s98
	s_and_b32 s2, s26, 2
	s_add_u32 s14, s50, 0x2660e000
	s_addc_u32 s15, s51, 0
	s_cmpk_lt_i32 s98, 0x100
	v_lshlrev_b32_e32 v4, 8, v0
	s_cselect_b64 s[0:1], -1, 0
	s_cmp_lg_u32 s2, 0
	v_bfe_u32 v1, v0, 5, 1
	v_and_b32_e32 v4, 0x1f00, v4
	v_lshlrev_b32_e32 v5, 4, v0
	s_movk_i32 s2, 0x80
	v_and_or_b32 v205, v5, s2, v4
	v_bitop3_b32 v213, v4, s2, v5 bitop3:0x34
	v_and_b32_e32 v4, 7, v0
	v_bitop3_b32 v5, v1, v0, 7 bitop3:0x78
	v_lshlrev_b32_e32 v214, 4, v5
	v_bitop3_b32 v5, v1, v4, 2 bitop3:0x36
	v_and_b32_e32 v175, 63, v0
	v_lshlrev_b32_e32 v215, 4, v5
	v_bitop3_b32 v5, v1, v4, 4 bitop3:0x36
	v_bitop3_b32 v4, v1, v4, 6 bitop3:0x36
	v_lshlrev_b32_e32 v216, 4, v5
	v_lshlrev_b32_e32 v217, 4, v4
	v_bfe_u32 v4, v175, 2, 2
	v_bfe_u32 v5, v175, 4, 1
	v_lshlrev_b32_e32 v1, 2, v1
	v_bfe_u32 v3, v0, 4, 2
	v_bitop3_b32 v7, v1, v5, v4 bitop3:0x36
	v_lshlrev_b32_e32 v218, 5, v7
	v_or_b32_e32 v7, 2, v3
	v_or_b32_e32 v3, 6, v3
	v_or_b32_e32 v6, v1, v4
	v_bitop3_b32 v7, v1, v7, v4 bitop3:0x36
	v_bitop3_b32 v1, v1, v3, v4 bitop3:0x36
	v_lshlrev_b32_e32 v221, 5, v1
	v_lshlrev_b32_e32 v1, 3, v0
	v_and_b32_e32 v176, 24, v1
	v_lshrrev_b32_e32 v1, 2, v0
	v_bfe_u32 v2, v0, 2, 4
	v_bitop3_b32 v5, v5, v6, 4 bitop3:0x36
	v_and_b32_e32 v159, 8, v1
	v_cndmask_b32_e64 v1, 0, 1, s[0:1]
	v_lshlrev_b32_e32 v219, 5, v7
	v_lshlrev_b32_e32 v220, 5, v5
	v_and_b32_e32 v174, 15, v0
	v_lshlrev_b32_e32 v177, 8, v6
	v_mov_b32_e32 v195, 0
	v_and_b32_e32 v194, 8, v2
	v_cmp_ne_u32_e64 s[2:3], 1, v1
	s_cbranch_scc1 .LBB0_1349
	s_and_b64 vcc, exec, s[2:3]
	v_readfirstlane_b32 s4, v0
	s_cbranch_vccnz .LBB0_1349
	s_add_u32 s0, s50, 0x304ae000
	s_addc_u32 s1, s51, 0
	v_lshrrev_b32_e32 v3, 3, v175
	s_and_b32 s6, s4, 0xffffffc0
	v_and_b32_e32 v178, 4, v3
	v_bitop3_b32 v179, v3, 4, v3 bitop3:0x3f
	v_or_b32_e32 v1, 3, v3
	v_or_b32_e32 v149, 11, v3
	v_or_b32_e32 v153, 19, v3
	v_or_b32_e32 v157, 27, v3
	v_or_b32_e32 v3, s6, v175
	v_add_u32_e32 v4, 0x200, v3
	v_ashrrev_i32_e32 v5, 4, v4
	v_lshlrev_b32_e32 v6, 1, v5
	s_movk_i32 s11, 0x2400
	v_bitop3_b32 v6, v6, v174, 14 bitop3:0x6c
	v_mul_lo_u32 v5, v5, s11
	v_lshl_or_b32 v160, v6, 4, v5
	v_ashrrev_i32_e32 v5, 4, v3
	v_lshlrev_b32_e32 v6, 1, v5
	v_bitop3_b32 v6, v6, v174, 14 bitop3:0x6c
	v_mul_lo_u32 v5, v5, s11
	v_lshl_or_b32 v162, v6, 4, v5
	v_ashrrev_i32_e32 v5, 31, v4
	v_lshrrev_b32_e32 v5, 28, v5
	v_add_u32_e32 v5, v4, v5
	v_ashrrev_i32_e32 v6, 4, v5
	v_and_b32_e32 v5, 0xffffff0, v5
	v_sub_u32_e32 v4, v4, v5
	v_bitop3_b32 v4, v6, v4, 15 bitop3:0x6c
	v_mul_lo_u32 v5, v6, s11
	v_lshl_add_u32 v164, v4, 4, v5
	v_ashrrev_i32_e32 v4, 31, v3
	v_lshrrev_b32_e32 v4, 28, v4
	v_add_u32_e32 v4, v3, v4
	v_ashrrev_i32_e32 v5, 4, v4
	v_and_b32_e32 v4, 0xffffff0, v4
	v_sub_u32_e32 v3, v3, v4
	s_lshr_b32 s16, s4, 7
	s_lshr_b32 s6, s4, 1
	s_lshl_b32 s4, s4, 4
	v_and_b32_e32 v2, 31, v0
	v_bitop3_b32 v3, v5, v3, 15 bitop3:0x6c
	v_mul_lo_u32 v4, v5, s11
	s_and_b32 s4, s4, 0xfffffc00
	v_lshl_add_u32 v166, v3, 4, v4
	v_and_or_b32 v181, s6, 32, v2
	s_add_i32 s17, s4, 0
	v_mov_b32_e32 v3, 0
	v_mbcnt_lo_u32_b32 v2, -1, 0
	v_or_b32_e32 v146, 2, v178
	v_or_b32_e32 v147, 9, v178
	v_or_b32_e32 v148, 8, v178
	v_or_b32_e32 v150, 10, v178
	v_or_b32_e32 v151, 17, v178
	v_or_b32_e32 v152, 16, v178
	v_or_b32_e32 v154, 18, v178
	v_or_b32_e32 v155, 25, v178
	v_or_b32_e32 v156, 24, v178
	v_or_b32_e32 v158, 26, v178
	s_mov_b32 s5, 0
	v_add3_u32 v180, 0, v177, v176
	v_mov_b32_e32 v167, v3
	v_mov_b32_e32 v165, v3
	v_mov_b32_e32 v163, v3
	v_mov_b32_e32 v161, v3
	v_mov_b64_e32 v[168:169], s[14:15]
	v_lshlrev_b32_e32 v170, 1, v159
	s_mov_b64 s[6:7], 0x800
	s_add_i32 s18, s17, 0x2000
	s_mov_b64 s[8:9], 0xa00
	s_add_i32 s19, s17, 0xc000
	s_add_i32 s27, s17, 0xe000
	s_movk_i32 s30, 0x101
	s_mov_b32 s10, 0x3e0293ee
	s_mov_b32 s31, 0x41000000
	s_mov_b32 s34, 0x3fb8aa3b
	s_mov_b32 s35, 0xc3e00000
	v_mov_b32_e32 v171, v3
	v_mov_b32_e32 v182, 0x64
	v_mov_b32_e32 v183, 0xf149f2ca
	v_mbcnt_hi_u32_b32 v184, -1, v2
	v_mov_b32_e32 v185, 0x43e00000
	s_mov_b32 s40, s98
	s_mov_b32 s41, s98
	s_branch .LBB0_1342

; #define LAS __attribute__((address_space(3)))
; DI void phase_attn_na(const Params& p, LAS unsigned char* lds, int G, int bid) {
;     const int tid = threadIdx.x, lane = tid & 63, wave = __builtin_amdgcn_readfirstlane(tid >> 6), h = lane >> 5;
;     const bf16_t* Z = (const bf16_t*)(p.ws + WS_Z);
;     bf16_t* Y = (bf16_t*)(p.ws + WS_Y);
;     LAS float* RPB = (LAS float*)(lds + AT4_XOFF);
;     const float c2 = 0.08838834764831845f * LOG2E;
;     const AtRd rd = at_rd_init<128>(lane);
;     const AtDma dm = at_dma_init<128>(L1IN * 2, wave, lane);
;     for (int u = bid; u < 256; u += G) {
;         NaDrv T; T.Z = (const char*)Z; T.RPB = RPB; T.b = u >> 6; T.head = (u >> 3) & 7; const int R = u & 7;
;         const int ra = 4 * R + 2 * (wave >> 2), ca = wave & 3;
;         T.r = ra + ((lane >> 4) & 1); T.c = 16 * ca + (lane & 15); const int qrow = NCTX + T.b * SEQ + 64 * T.r + T.c;
;         T.r0 = min(max(T.r - 4, 0), 24); T.c0 = min(max(T.c - 8, 0), 48);
;         T.koff = ca == 0 ? 0 : (ca == 1 ? 8 : (ca == 2 ? 24 : 32));
;         T.wr0 = min(max(ra - 4, 0), 24); T.wr1 = min(max(ra + 1 - 4, 0), 24) + 7;
;         T.rlo = min(max(4 * R - 4, 0), 24);
;         const int rhi = min(max(4 * R + 3 - 4, 0), 24) + 7;
;         const int ntl = 4 + (rhi - T.rlo + 1);
;         __syncthreads();
;         for (int i = tid; i < 15 * 31; i += NTHREADS) RPB[i] = p.in[33][T.head * 465 + i];
.LBB0_1349:
	s_bitcmp1_b32 s26, 2
	s_waitcnt vmcnt(0) lgkmcnt(0)
	s_barrier
	s_cbranch_scc1 .LBB0_1381
	s_and_b64 vcc, exec, s[2:3]
	v_readfirstlane_b32 s0, v0
	s_cbranch_vccnz .LBB0_1381
	s_movk_i32 s1, 0x1d1
	v_cmp_gt_u32_e64 s[2:3], s1, v0
	s_add_i32 s1, 0, 0x1e000
	v_lshrrev_b32_e32 v1, 3, v0
	v_lshl_add_u32 v226, v0, 2, s1
	s_and_b32 s1, s0, 0xffffffc0
	v_and_b32_e32 v225, 4, v1
	v_or_b32_e32 v1, s1, v175
	v_add_u32_e32 v2, 0x200, v1
	v_ashrrev_i32_e32 v3, 4, v2
	v_lshlrev_b32_e32 v4, 1, v3
	s_movk_i32 s19, 0x2400
	v_bitop3_b32 v4, v4, v174, 14 bitop3:0x6c
	v_mul_lo_u32 v3, v3, s19
	v_lshl_or_b32 v196, v4, 4, v3
	v_ashrrev_i32_e32 v3, 4, v1
	v_lshlrev_b32_e32 v4, 1, v3
	v_bitop3_b32 v4, v4, v174, 14 bitop3:0x6c
	v_mul_lo_u32 v3, v3, s19
	v_lshl_or_b32 v198, v4, 4, v3
	v_ashrrev_i32_e32 v3, 31, v2
	v_lshrrev_b32_e32 v3, 28, v3
	v_add_u32_e32 v3, v2, v3
	v_ashrrev_i32_e32 v4, 4, v3
	v_and_b32_e32 v3, 0xffffff0, v3
	v_sub_u32_e32 v2, v2, v3
	v_bitop3_b32 v2, v4, v2, 15 bitop3:0x6c
	v_mul_lo_u32 v3, v4, s19
	v_lshl_add_u32 v200, v2, 4, v3
	v_ashrrev_i32_e32 v2, 31, v1
	v_lshrrev_b32_e32 v2, 28, v2
	s_lshr_b32 s4, s0, 7
	v_add_u32_e32 v2, v1, v2
	s_lshr_b32 s1, s0, 6
	s_and_b32 s27, s4, 0x1fffffe
	s_bfe_u32 s31, s0, 0x20006
	v_ashrrev_i32_e32 v3, 4, v2
	v_and_b32_e32 v2, 0xffffff0, v2
	s_cmp_eq_u32 s31, 2
	v_sub_u32_e32 v1, v1, v2
	s_cselect_b32 s36, 24, 32
	s_lshl_b32 s1, s1, 10
	v_bfe_u32 v224, v0, 4, 1
	v_bitop3_b32 v1, v3, v1, 15 bitop3:0x6c
	v_mul_lo_u32 v2, v3, s19
	s_add_i32 s37, s1, 0
	v_lshrrev_b32_e32 v3, 1, v0
	s_lshl_b32 s1, s31, 6
	s_lshr_b32 s0, s0, 8
	v_and_b32_e32 v229, 16, v3
	v_lshl_or_b32 v3, v174, 2, s1
	v_mul_u32_u24_e32 v4, 0x7c, v224
	s_mulk_i32 s0, 0xf8
	v_lshl_add_u32 v202, v1, 4, v2
	v_lshl_or_b32 v1, s31, 4, v174
	v_add3_u32 v3, v3, v4, s0
	v_sub_u32_e64 v2, v1, 8 clamp
	v_sub_u32_e32 v3, 0, v3
	v_min_u32_e32 v204, 48, v2
	v_mov_b32_e32 v2, 0
	v_add_u32_e32 v230, 0x1dfc0, v3
	v_mbcnt_lo_u32_b32 v3, -1, 0
	v_or_b32_e32 v223, v177, v176
	s_mov_b32 s17, 0
	v_mov_b32_e32 v203, v2
	v_mov_b32_e32 v201, v2
	v_mov_b32_e32 v199, v2
	v_mov_b32_e32 v197, v2
	v_add_u32_e32 v227, 16, v204
	v_or_b32_e32 v228, 0x400, v1
	v_mov_b32_e32 v1, v204
	s_lshl_b32 s40, s98, 2
	s_lshl_b32 s41, s23, 2
	v_mov_b64_e32 v[206:207], s[14:15]
	v_lshlrev_b32_e32 v208, 1, v159
	v_mov_b32_e32 v209, v2
	s_add_i32 s52, s37, 0x2000
	s_add_i32 s53, s37, 0xc000
	s_add_i32 s54, s37, 0xe000
	s_mov_b32 s18, 0x3e0293ee
	s_mov_b32 s55, 0xff800000
	s_mov_b32 s56, 0x41000000
	s_mov_b32 s30, 0x3fb8aa3b
	s_mov_b32 s57, 0xc3e00000
	s_mov_b64 s[34:35], 0x304ae400
	s_mov_b32 s58, 0x304ae000
	v_mov_b32_e32 v231, 0xf149f2ca
	v_mbcnt_hi_u32_b32 v232, -1, v3
	v_mov_b32_e32 v233, 0x43e00000
	s_mov_b32 s59, s98
	s_branch .LBB0_1354
